# router phase prologue: first-row and router-bias loads issued before the (now pipelined) router-weight loads
# speedup vs baseline: 1.0033x; 1.0033x over previous
; __device__ __forceinline__ unsigned cvt_pk_bf16(float lo, float hi) { unsigned r; asm volatile("v_cvt_pk_bf16_f32 %0, %1, %2" : "=v"(r) : "v"(lo), "v"(hi)); return r; }
; __device__ __forceinline__ void phase5(Frame& F, const Args& a) {
;     ...
;     int li = 0;
;     bf16x8_t wh[8][2], wl[8][2];
;     { const float* wp = a.rw + (size_t)(wid * 256 + 8 * (lane >> 4)) * NE + (lane & 15);
; #pragma unroll
;         for (int sk = 0; sk < 8; ++sk)
; #pragma unroll
;             for (int nt = 0; nt < 2; ++nt) { float w8[8];
; #pragma unroll
;                 for (int t = 0; t < 8; ++t) w8[t] = wp[(size_t)(32 * sk + t) * NE + 16 * nt];
;                 pg8::u32x4 hv, lv;
; #pragma unroll
;                 for (int t2 = 0; t2 < 4; ++t2) { const unsigned h = pg8::cvt_pk_bf16(w8[2 * t2], w8[2 * t2 + 1]); hv[t2] = h; lv[t2] = pg8::cvt_pk_bf16(w8[2 * t2] - bflo(h), w8[2 * t2 + 1] - bfhi(h)); }
;                 wh[sk][nt] = __builtin_bit_cast(bf16x8_t, hv); wl[sk][nt] = __builtin_bit_cast(bf16x8_t, lv); } }
;     const float rbv = a.rb[lane & 31];
;     v2u ynx[8];
; #pragma unroll
;     for (int j = 0; j < 8; ++j) ynx[j] = *((const v2u*)(Y1 + (size_t)(row_base + wid) * D) + lane + 64 * j);
.LBB0_624:
	s_or_b64 exec, exec, s[0:1]
	s_add_u32 s12, s76, 0x20000000
	s_addc_u32 s13, s77, 0
	s_lshl_b32 s0, s49, 8
	v_bfe_u32 v131, v138, 4, 2
	v_readlane_b32 s52, v251, 2
	v_lshl_or_b32 v140, v131, 3, s0
	v_mov_b32_e32 v141, 0
	v_readlane_b32 s62, v251, 12
	v_readlane_b32 s63, v251, 13
	s_waitcnt vmcnt(19)
	v_lshlrev_b64 v[2:3], 7, v[140:141]
	s_mov_b64 s[14:15], s[62:63]
	v_and_b32_e32 v132, 15, v138
	v_lshl_add_u64 v[2:3], s[14:15], 0, v[2:3]
	v_lshlrev_b32_e32 v4, 2, v132
	v_mov_b32_e32 v5, v141
	s_waitcnt vmcnt(5)
	v_lshl_add_u64 v[106:107], v[2:3], 0, v[4:5]
	s_movk_i32 s0, 0x1000
	v_add_co_u32_e32 v26, vcc, s0, v106
	s_movk_i32 s1, 0x2000
	s_nop 1
	v_addc_co_u32_e32 v27, vcc, 0, v107, vcc
	v_add_co_u32_e32 v42, vcc, s1, v106
	s_movk_i32 s0, 0x3000
	s_nop 1
	v_addc_co_u32_e32 v43, vcc, 0, v107, vcc
	v_add_co_u32_e32 v58, vcc, s0, v106
	s_movk_i32 s1, 0x4000
	s_nop 1
	v_addc_co_u32_e32 v59, vcc, 0, v107, vcc
	v_add_co_u32_e32 v74, vcc, s1, v106
	s_movk_i32 s0, 0x5000
	s_nop 1
	v_addc_co_u32_e32 v75, vcc, 0, v107, vcc
	v_add_co_u32_e32 v90, vcc, s0, v106
	s_movk_i32 s1, 0x6000
	s_nop 1
	v_addc_co_u32_e32 v91, vcc, 0, v107, vcc
	v_add_co_u32_e32 v108, vcc, s1, v106
	s_movk_i32 s0, 0x7000
	s_nop 1
	v_addc_co_u32_e32 v109, vcc, 0, v107, vcc
	s_waitcnt vmcnt(1)
	v_add_co_u32_e32 v122, vcc, s0, v106
	s_add_i32 s0, s18, s49
	s_nop 1
	v_addc_co_u32_e32 v123, vcc, 0, v107, vcc
	s_ashr_i32 s1, s0, 31
	s_lshl_b64 s[4:5], s[0:1], 12
	v_readlane_b32 s64, v251, 14
	v_readlane_b32 s65, v251, 15
	v_and_b32_e32 v133, 63, v138
	s_add_u32 s4, s12, s4
	v_lshlrev_b32_e32 v130, 3, v133
	s_addc_u32 s5, s13, s5
	s_mov_b32 s1, 8
	s_mov_b32 s31, 0xffff0000
	s_mov_b32 s10, 0
	s_cmp_gt_i32 s30, 0
	v_readlane_b32 s53, v251, 3
	v_readlane_b32 s54, v251, 4
	v_readlane_b32 s55, v251, 5
	v_readlane_b32 s56, v251, 6
	v_readlane_b32 s57, v251, 7
	v_readlane_b32 s58, v251, 8
	v_readlane_b32 s59, v251, 9
	v_readlane_b32 s60, v251, 10
	v_readlane_b32 s61, v251, 11
	v_readlane_b32 s66, v251, 16
	v_readlane_b32 s67, v251, 17
	v_and_b32_e32 v1, 31, v138
	v_lshlrev_b32_e32 v137, 2, v1
	global_load_dword v139, v137, s[64:65]
	global_load_dwordx2 v[142:143], v130, s[4:5]
	global_load_dwordx2 v[144:145], v130, s[4:5] offset:512
	global_load_dwordx2 v[146:147], v130, s[4:5] offset:1024
	global_load_dwordx2 v[148:149], v130, s[4:5] offset:1536
	global_load_dwordx2 v[150:151], v130, s[4:5] offset:2048
	global_load_dwordx2 v[152:153], v130, s[4:5] offset:2560
	global_load_dwordx2 v[154:155], v130, s[4:5] offset:3072
	global_load_dwordx2 v[156:157], v130, s[4:5] offset:3584
	v_mov_b32_e32 v244, v106
	v_mov_b32_e32 v245, v107
	v_mov_b32_e32 v252, 0x1000
	v_mov_b32_e32 v253, 0
	global_load_dword v2, v[244:245], off
	global_load_dword v3, v[244:245], off offset:128
	global_load_dword v4, v[244:245], off offset:256
	global_load_dword v5, v[244:245], off offset:384
	global_load_dword v6, v[244:245], off offset:512
	global_load_dword v7, v[244:245], off offset:640
	global_load_dword v8, v[244:245], off offset:768
	global_load_dword v9, v[244:245], off offset:896
	global_load_dword v10, v[244:245], off offset:64
	global_load_dword v11, v[244:245], off offset:192
	global_load_dword v12, v[244:245], off offset:320
	global_load_dword v13, v[244:245], off offset:448
	global_load_dword v14, v[244:245], off offset:576
	global_load_dword v15, v[244:245], off offset:704
	global_load_dword v16, v[244:245], off offset:832
	global_load_dword v17, v[244:245], off offset:960
	v_lshl_add_u64 v[244:245], v[244:245], 0, v[252:253]
	global_load_dword v18, v[244:245], off
	global_load_dword v19, v[244:245], off offset:128
	global_load_dword v20, v[244:245], off offset:256
	global_load_dword v21, v[244:245], off offset:384
	global_load_dword v22, v[244:245], off offset:512
	global_load_dword v23, v[244:245], off offset:640
	global_load_dword v24, v[244:245], off offset:768
	global_load_dword v25, v[244:245], off offset:896
	global_load_dword v26, v[244:245], off offset:64
	global_load_dword v27, v[244:245], off offset:192
	global_load_dword v28, v[244:245], off offset:320
	global_load_dword v29, v[244:245], off offset:448
	global_load_dword v30, v[244:245], off offset:576
	global_load_dword v31, v[244:245], off offset:704
	global_load_dword v32, v[244:245], off offset:832
	global_load_dword v33, v[244:245], off offset:960
	v_lshl_add_u64 v[244:245], v[244:245], 0, v[252:253]
	global_load_dword v34, v[244:245], off
	global_load_dword v35, v[244:245], off offset:128
	global_load_dword v36, v[244:245], off offset:256
	global_load_dword v37, v[244:245], off offset:384
	global_load_dword v38, v[244:245], off offset:512
	global_load_dword v39, v[244:245], off offset:640
	global_load_dword v40, v[244:245], off offset:768
	global_load_dword v41, v[244:245], off offset:896
	global_load_dword v42, v[244:245], off offset:64
	global_load_dword v43, v[244:245], off offset:192
	global_load_dword v44, v[244:245], off offset:320
	global_load_dword v45, v[244:245], off offset:448
	global_load_dword v46, v[244:245], off offset:576
	global_load_dword v47, v[244:245], off offset:704
	global_load_dword v48, v[244:245], off offset:832
	global_load_dword v49, v[244:245], off offset:960
	v_lshl_add_u64 v[244:245], v[244:245], 0, v[252:253]
	s_waitcnt vmcnt(40)
; __device__ __forceinline__ unsigned cvt_pk_bf16(float lo, float hi) { unsigned r; asm volatile("v_cvt_pk_bf16_f32 %0, %1, %2" : "=v"(r) : "v"(lo), "v"(hi)); return r; }
; __device__ __forceinline__ void phase5(Frame& F, const Args& a) {
;     ...
; #pragma unroll
;         for (int sk = 0; sk < 8; ++sk)
; #pragma unroll
;             for (int nt = 0; nt < 2; ++nt) { float w8[8];
; #pragma unroll
;                 for (int t = 0; t < 8; ++t) w8[t] = wp[(size_t)(32 * sk + t) * NE + 16 * nt];
;                 pg8::u32x4 hv, lv;
; #pragma unroll
;                 for (int t2 = 0; t2 < 4; ++t2) { const unsigned h = pg8::cvt_pk_bf16(w8[2 * t2], w8[2 * t2 + 1]); hv[t2] = h; lv[t2] = pg8::cvt_pk_bf16(w8[2 * t2] - bflo(h), w8[2 * t2 + 1] - bfhi(h)); }
;                 wh[sk][nt] = __builtin_bit_cast(bf16x8_t, hv); wl[sk][nt] = __builtin_bit_cast(bf16x8_t, lv); } }
	v_cvt_pk_bf16_f32 v243, v2, v3
	s_nop 0
	v_lshlrev_b32_e32 v249, 16, v243
	v_and_b32_e32 v250, 0xffff0000, v243
	v_sub_f32_e32 v249, v2, v249
	v_sub_f32_e32 v250, v3, v250
	v_cvt_pk_bf16_f32 v246, v249, v250
	v_cvt_pk_bf16_f32 v3, v4, v5
	s_nop 0
	v_lshlrev_b32_e32 v249, 16, v3
	v_and_b32_e32 v250, 0xffff0000, v3
	v_sub_f32_e32 v249, v4, v249
	v_sub_f32_e32 v250, v5, v250
	v_cvt_pk_bf16_f32 v247, v249, v250
	v_cvt_pk_bf16_f32 v4, v6, v7
	s_nop 0
	v_lshlrev_b32_e32 v249, 16, v4
	v_and_b32_e32 v250, 0xffff0000, v4
	v_sub_f32_e32 v249, v6, v249
	v_sub_f32_e32 v250, v7, v250
	v_cvt_pk_bf16_f32 v248, v249, v250
	v_cvt_pk_bf16_f32 v5, v8, v9
	s_nop 0
	v_lshlrev_b32_e32 v249, 16, v5
	v_and_b32_e32 v250, 0xffff0000, v5
	v_sub_f32_e32 v249, v8, v249
	v_sub_f32_e32 v250, v9, v250
	v_cvt_pk_bf16_f32 v9, v249, v250
	v_mov_b32_e32 v2, v243
	v_mov_b32_e32 v6, v246
	v_mov_b32_e32 v7, v247
	v_mov_b32_e32 v8, v248
	global_load_dword v50, v[244:245], off
	global_load_dword v51, v[244:245], off offset:128
	global_load_dword v52, v[244:245], off offset:256
	global_load_dword v53, v[244:245], off offset:384
	global_load_dword v54, v[244:245], off offset:512
	global_load_dword v55, v[244:245], off offset:640
	global_load_dword v56, v[244:245], off offset:768
	global_load_dword v57, v[244:245], off offset:896
	s_waitcnt vmcnt(40)
	v_cvt_pk_bf16_f32 v243, v10, v11
	s_nop 0
	v_lshlrev_b32_e32 v249, 16, v243
	v_and_b32_e32 v250, 0xffff0000, v243
	v_sub_f32_e32 v249, v10, v249
	v_sub_f32_e32 v250, v11, v250
	v_cvt_pk_bf16_f32 v246, v249, v250
	v_cvt_pk_bf16_f32 v11, v12, v13
	s_nop 0
	v_lshlrev_b32_e32 v249, 16, v11
	v_and_b32_e32 v250, 0xffff0000, v11
	v_sub_f32_e32 v249, v12, v249
	v_sub_f32_e32 v250, v13, v250
	v_cvt_pk_bf16_f32 v247, v249, v250
	v_cvt_pk_bf16_f32 v12, v14, v15
	s_nop 0
	v_lshlrev_b32_e32 v249, 16, v12
	v_and_b32_e32 v250, 0xffff0000, v12
	v_sub_f32_e32 v249, v14, v249
	v_sub_f32_e32 v250, v15, v250
	v_cvt_pk_bf16_f32 v248, v249, v250
	v_cvt_pk_bf16_f32 v13, v16, v17
	s_nop 0
	v_lshlrev_b32_e32 v249, 16, v13
	v_and_b32_e32 v250, 0xffff0000, v13
	v_sub_f32_e32 v249, v16, v249
	v_sub_f32_e32 v250, v17, v250
	v_cvt_pk_bf16_f32 v17, v249, v250
	v_mov_b32_e32 v10, v243
	v_mov_b32_e32 v14, v246
	v_mov_b32_e32 v15, v247
	v_mov_b32_e32 v16, v248
	global_load_dword v58, v[244:245], off offset:64
	global_load_dword v59, v[244:245], off offset:192
	global_load_dword v60, v[244:245], off offset:320
	global_load_dword v61, v[244:245], off offset:448
	global_load_dword v62, v[244:245], off offset:576
	global_load_dword v63, v[244:245], off offset:704
	global_load_dword v64, v[244:245], off offset:832
	global_load_dword v65, v[244:245], off offset:960
	v_lshl_add_u64 v[244:245], v[244:245], 0, v[252:253]
	s_waitcnt vmcnt(40)
	v_cvt_pk_bf16_f32 v243, v18, v19
	s_nop 0
	v_lshlrev_b32_e32 v249, 16, v243
	v_and_b32_e32 v250, 0xffff0000, v243
	v_sub_f32_e32 v249, v18, v249
	v_sub_f32_e32 v250, v19, v250
	v_cvt_pk_bf16_f32 v246, v249, v250
	v_cvt_pk_bf16_f32 v19, v20, v21
	s_nop 0
	v_lshlrev_b32_e32 v249, 16, v19
	v_and_b32_e32 v250, 0xffff0000, v19
	v_sub_f32_e32 v249, v20, v249
	v_sub_f32_e32 v250, v21, v250
	v_cvt_pk_bf16_f32 v247, v249, v250
	v_cvt_pk_bf16_f32 v20, v22, v23
	s_nop 0
	v_lshlrev_b32_e32 v249, 16, v20
	v_and_b32_e32 v250, 0xffff0000, v20
	v_sub_f32_e32 v249, v22, v249
	v_sub_f32_e32 v250, v23, v250
	v_cvt_pk_bf16_f32 v248, v249, v250
	v_cvt_pk_bf16_f32 v21, v24, v25
	s_nop 0
	v_lshlrev_b32_e32 v249, 16, v21
	v_and_b32_e32 v250, 0xffff0000, v21
	v_sub_f32_e32 v249, v24, v249
	v_sub_f32_e32 v250, v25, v250
	v_cvt_pk_bf16_f32 v25, v249, v250
	v_mov_b32_e32 v18, v243
	v_mov_b32_e32 v22, v246
	v_mov_b32_e32 v23, v247
	v_mov_b32_e32 v24, v248
	global_load_dword v66, v[244:245], off
	global_load_dword v67, v[244:245], off offset:128
	global_load_dword v68, v[244:245], off offset:256
	global_load_dword v69, v[244:245], off offset:384
	global_load_dword v70, v[244:245], off offset:512
	global_load_dword v71, v[244:245], off offset:640
	global_load_dword v72, v[244:245], off offset:768
	global_load_dword v73, v[244:245], off offset:896
	s_waitcnt vmcnt(40)
	v_cvt_pk_bf16_f32 v243, v26, v27
	s_nop 0
	v_lshlrev_b32_e32 v249, 16, v243
	v_and_b32_e32 v250, 0xffff0000, v243
	v_sub_f32_e32 v249, v26, v249
	v_sub_f32_e32 v250, v27, v250
	v_cvt_pk_bf16_f32 v246, v249, v250
	v_cvt_pk_bf16_f32 v27, v28, v29
	s_nop 0
	v_lshlrev_b32_e32 v249, 16, v27
	v_and_b32_e32 v250, 0xffff0000, v27
	v_sub_f32_e32 v249, v28, v249
	v_sub_f32_e32 v250, v29, v250
	v_cvt_pk_bf16_f32 v247, v249, v250
	v_cvt_pk_bf16_f32 v28, v30, v31
	s_nop 0
	v_lshlrev_b32_e32 v249, 16, v28
	v_and_b32_e32 v250, 0xffff0000, v28
	v_sub_f32_e32 v249, v30, v249
	v_sub_f32_e32 v250, v31, v250
	v_cvt_pk_bf16_f32 v248, v249, v250
	v_cvt_pk_bf16_f32 v29, v32, v33
	s_nop 0
	v_lshlrev_b32_e32 v249, 16, v29
	v_and_b32_e32 v250, 0xffff0000, v29
	v_sub_f32_e32 v249, v32, v249
	v_sub_f32_e32 v250, v33, v250
	v_cvt_pk_bf16_f32 v33, v249, v250
	v_mov_b32_e32 v26, v243
	v_mov_b32_e32 v30, v246
	v_mov_b32_e32 v31, v247
	v_mov_b32_e32 v32, v248
	global_load_dword v74, v[244:245], off offset:64
	global_load_dword v75, v[244:245], off offset:192
	global_load_dword v76, v[244:245], off offset:320
	global_load_dword v77, v[244:245], off offset:448
	global_load_dword v78, v[244:245], off offset:576
	global_load_dword v79, v[244:245], off offset:704
	global_load_dword v80, v[244:245], off offset:832
	global_load_dword v81, v[244:245], off offset:960
	v_lshl_add_u64 v[244:245], v[244:245], 0, v[252:253]
	s_waitcnt vmcnt(40)
; __device__ __forceinline__ unsigned cvt_pk_bf16(float lo, float hi) { unsigned r; asm volatile("v_cvt_pk_bf16_f32 %0, %1, %2" : "=v"(r) : "v"(lo), "v"(hi)); return r; }
; __device__ __forceinline__ void phase5(Frame& F, const Args& a) {
;     ...
; #pragma unroll
;         for (int sk = 0; sk < 8; ++sk)
; #pragma unroll
;             for (int nt = 0; nt < 2; ++nt) { float w8[8];
; #pragma unroll
;                 for (int t = 0; t < 8; ++t) w8[t] = wp[(size_t)(32 * sk + t) * NE + 16 * nt];
;                 pg8::u32x4 hv, lv;
; #pragma unroll
;                 for (int t2 = 0; t2 < 4; ++t2) { const unsigned h = pg8::cvt_pk_bf16(w8[2 * t2], w8[2 * t2 + 1]); hv[t2] = h; lv[t2] = pg8::cvt_pk_bf16(w8[2 * t2] - bflo(h), w8[2 * t2 + 1] - bfhi(h)); }
;                 wh[sk][nt] = __builtin_bit_cast(bf16x8_t, hv); wl[sk][nt] = __builtin_bit_cast(bf16x8_t, lv); } }
	v_cvt_pk_bf16_f32 v243, v34, v35
	s_nop 0
	v_lshlrev_b32_e32 v249, 16, v243
	v_and_b32_e32 v250, 0xffff0000, v243
	v_sub_f32_e32 v249, v34, v249
	v_sub_f32_e32 v250, v35, v250
	v_cvt_pk_bf16_f32 v246, v249, v250
	v_cvt_pk_bf16_f32 v35, v36, v37
	s_nop 0
	v_lshlrev_b32_e32 v249, 16, v35
	v_and_b32_e32 v250, 0xffff0000, v35
	v_sub_f32_e32 v249, v36, v249
	v_sub_f32_e32 v250, v37, v250
	v_cvt_pk_bf16_f32 v247, v249, v250
	v_cvt_pk_bf16_f32 v36, v38, v39
	s_nop 0
	v_lshlrev_b32_e32 v249, 16, v36
	v_and_b32_e32 v250, 0xffff0000, v36
	v_sub_f32_e32 v249, v38, v249
	v_sub_f32_e32 v250, v39, v250
	v_cvt_pk_bf16_f32 v248, v249, v250
	v_cvt_pk_bf16_f32 v37, v40, v41
	s_nop 0
	v_lshlrev_b32_e32 v249, 16, v37
	v_and_b32_e32 v250, 0xffff0000, v37
	v_sub_f32_e32 v249, v40, v249
	v_sub_f32_e32 v250, v41, v250
	v_cvt_pk_bf16_f32 v41, v249, v250
	v_mov_b32_e32 v34, v243
	v_mov_b32_e32 v38, v246
	v_mov_b32_e32 v39, v247
	v_mov_b32_e32 v40, v248
	global_load_dword v82, v[244:245], off
	global_load_dword v83, v[244:245], off offset:128
	global_load_dword v84, v[244:245], off offset:256
	global_load_dword v85, v[244:245], off offset:384
	global_load_dword v86, v[244:245], off offset:512
	global_load_dword v87, v[244:245], off offset:640
	global_load_dword v88, v[244:245], off offset:768
	global_load_dword v89, v[244:245], off offset:896
	s_waitcnt vmcnt(40)
	v_cvt_pk_bf16_f32 v243, v42, v43
	s_nop 0
	v_lshlrev_b32_e32 v249, 16, v243
	v_and_b32_e32 v250, 0xffff0000, v243
	v_sub_f32_e32 v249, v42, v249
	v_sub_f32_e32 v250, v43, v250
	v_cvt_pk_bf16_f32 v246, v249, v250
	v_cvt_pk_bf16_f32 v43, v44, v45
	s_nop 0
	v_lshlrev_b32_e32 v249, 16, v43
	v_and_b32_e32 v250, 0xffff0000, v43
	v_sub_f32_e32 v249, v44, v249
	v_sub_f32_e32 v250, v45, v250
	v_cvt_pk_bf16_f32 v247, v249, v250
	v_cvt_pk_bf16_f32 v44, v46, v47
	s_nop 0
	v_lshlrev_b32_e32 v249, 16, v44
	v_and_b32_e32 v250, 0xffff0000, v44
	v_sub_f32_e32 v249, v46, v249
	v_sub_f32_e32 v250, v47, v250
	v_cvt_pk_bf16_f32 v248, v249, v250
	v_cvt_pk_bf16_f32 v45, v48, v49
	s_nop 0
	v_lshlrev_b32_e32 v249, 16, v45
	v_and_b32_e32 v250, 0xffff0000, v45
	v_sub_f32_e32 v249, v48, v249
	v_sub_f32_e32 v250, v49, v250
	v_cvt_pk_bf16_f32 v49, v249, v250
	v_mov_b32_e32 v42, v243
	v_mov_b32_e32 v46, v246
	v_mov_b32_e32 v47, v247
	v_mov_b32_e32 v48, v248
	global_load_dword v90, v[244:245], off offset:64
	global_load_dword v91, v[244:245], off offset:192
	global_load_dword v92, v[244:245], off offset:320
	global_load_dword v93, v[244:245], off offset:448
	global_load_dword v94, v[244:245], off offset:576
	global_load_dword v95, v[244:245], off offset:704
	global_load_dword v96, v[244:245], off offset:832
	global_load_dword v97, v[244:245], off offset:960
	v_lshl_add_u64 v[244:245], v[244:245], 0, v[252:253]
	s_waitcnt vmcnt(40)
	v_cvt_pk_bf16_f32 v243, v50, v51
	s_nop 0
	v_lshlrev_b32_e32 v249, 16, v243
	v_and_b32_e32 v250, 0xffff0000, v243
	v_sub_f32_e32 v249, v50, v249
	v_sub_f32_e32 v250, v51, v250
	v_cvt_pk_bf16_f32 v246, v249, v250
	v_cvt_pk_bf16_f32 v51, v52, v53
	s_nop 0
	v_lshlrev_b32_e32 v249, 16, v51
	v_and_b32_e32 v250, 0xffff0000, v51
	v_sub_f32_e32 v249, v52, v249
	v_sub_f32_e32 v250, v53, v250
	v_cvt_pk_bf16_f32 v247, v249, v250
	v_cvt_pk_bf16_f32 v52, v54, v55
	s_nop 0
	v_lshlrev_b32_e32 v249, 16, v52
	v_and_b32_e32 v250, 0xffff0000, v52
	v_sub_f32_e32 v249, v54, v249
	v_sub_f32_e32 v250, v55, v250
	v_cvt_pk_bf16_f32 v248, v249, v250
	v_cvt_pk_bf16_f32 v53, v56, v57
	s_nop 0
	v_lshlrev_b32_e32 v249, 16, v53
	v_and_b32_e32 v250, 0xffff0000, v53
	v_sub_f32_e32 v249, v56, v249
	v_sub_f32_e32 v250, v57, v250
	v_cvt_pk_bf16_f32 v57, v249, v250
	v_mov_b32_e32 v50, v243
	v_mov_b32_e32 v54, v246
	v_mov_b32_e32 v55, v247
	v_mov_b32_e32 v56, v248
	global_load_dword v98, v[244:245], off
	global_load_dword v99, v[244:245], off offset:128
	global_load_dword v100, v[244:245], off offset:256
	global_load_dword v101, v[244:245], off offset:384
	global_load_dword v102, v[244:245], off offset:512
	global_load_dword v103, v[244:245], off offset:640
	global_load_dword v104, v[244:245], off offset:768
	global_load_dword v105, v[244:245], off offset:896
	s_waitcnt vmcnt(40)
	v_cvt_pk_bf16_f32 v243, v58, v59
	s_nop 0
	v_lshlrev_b32_e32 v249, 16, v243
	v_and_b32_e32 v250, 0xffff0000, v243
	v_sub_f32_e32 v249, v58, v249
	v_sub_f32_e32 v250, v59, v250
	v_cvt_pk_bf16_f32 v246, v249, v250
	v_cvt_pk_bf16_f32 v59, v60, v61
	s_nop 0
	v_lshlrev_b32_e32 v249, 16, v59
	v_and_b32_e32 v250, 0xffff0000, v59
	v_sub_f32_e32 v249, v60, v249
	v_sub_f32_e32 v250, v61, v250
	v_cvt_pk_bf16_f32 v247, v249, v250
	v_cvt_pk_bf16_f32 v60, v62, v63
	s_nop 0
	v_lshlrev_b32_e32 v249, 16, v60
	v_and_b32_e32 v250, 0xffff0000, v60
	v_sub_f32_e32 v249, v62, v249
	v_sub_f32_e32 v250, v63, v250
	v_cvt_pk_bf16_f32 v248, v249, v250
	v_cvt_pk_bf16_f32 v61, v64, v65
	s_nop 0
	v_lshlrev_b32_e32 v249, 16, v61
	v_and_b32_e32 v250, 0xffff0000, v61
	v_sub_f32_e32 v249, v64, v249
	v_sub_f32_e32 v250, v65, v250
	v_cvt_pk_bf16_f32 v65, v249, v250
	v_mov_b32_e32 v58, v243
	v_mov_b32_e32 v62, v246
	v_mov_b32_e32 v63, v247
	v_mov_b32_e32 v64, v248
	global_load_dword v106, v[244:245], off offset:64
	global_load_dword v107, v[244:245], off offset:192
	global_load_dword v108, v[244:245], off offset:320
	global_load_dword v109, v[244:245], off offset:448
	global_load_dword v110, v[244:245], off offset:576
	global_load_dword v111, v[244:245], off offset:704
	global_load_dword v112, v[244:245], off offset:832
	global_load_dword v113, v[244:245], off offset:960
	v_lshl_add_u64 v[244:245], v[244:245], 0, v[252:253]
	s_waitcnt vmcnt(40)
; __device__ __forceinline__ unsigned cvt_pk_bf16(float lo, float hi) { unsigned r; asm volatile("v_cvt_pk_bf16_f32 %0, %1, %2" : "=v"(r) : "v"(lo), "v"(hi)); return r; }
; __device__ __forceinline__ void phase5(Frame& F, const Args& a) {
;     ...
; #pragma unroll
;         for (int sk = 0; sk < 8; ++sk)
; #pragma unroll
;             for (int nt = 0; nt < 2; ++nt) { float w8[8];
; #pragma unroll
;                 for (int t = 0; t < 8; ++t) w8[t] = wp[(size_t)(32 * sk + t) * NE + 16 * nt];
;                 pg8::u32x4 hv, lv;
; #pragma unroll
;                 for (int t2 = 0; t2 < 4; ++t2) { const unsigned h = pg8::cvt_pk_bf16(w8[2 * t2], w8[2 * t2 + 1]); hv[t2] = h; lv[t2] = pg8::cvt_pk_bf16(w8[2 * t2] - bflo(h), w8[2 * t2 + 1] - bfhi(h)); }
;                 wh[sk][nt] = __builtin_bit_cast(bf16x8_t, hv); wl[sk][nt] = __builtin_bit_cast(bf16x8_t, lv); } }
	v_cvt_pk_bf16_f32 v243, v66, v67
	s_nop 0
	v_lshlrev_b32_e32 v249, 16, v243
	v_and_b32_e32 v250, 0xffff0000, v243
	v_sub_f32_e32 v249, v66, v249
	v_sub_f32_e32 v250, v67, v250
	v_cvt_pk_bf16_f32 v246, v249, v250
	v_cvt_pk_bf16_f32 v67, v68, v69
	s_nop 0
	v_lshlrev_b32_e32 v249, 16, v67
	v_and_b32_e32 v250, 0xffff0000, v67
	v_sub_f32_e32 v249, v68, v249
	v_sub_f32_e32 v250, v69, v250
	v_cvt_pk_bf16_f32 v247, v249, v250
	v_cvt_pk_bf16_f32 v68, v70, v71
	s_nop 0
	v_lshlrev_b32_e32 v249, 16, v68
	v_and_b32_e32 v250, 0xffff0000, v68
	v_sub_f32_e32 v249, v70, v249
	v_sub_f32_e32 v250, v71, v250
	v_cvt_pk_bf16_f32 v248, v249, v250
	v_cvt_pk_bf16_f32 v69, v72, v73
	s_nop 0
	v_lshlrev_b32_e32 v249, 16, v69
	v_and_b32_e32 v250, 0xffff0000, v69
	v_sub_f32_e32 v249, v72, v249
	v_sub_f32_e32 v250, v73, v250
	v_cvt_pk_bf16_f32 v73, v249, v250
	v_mov_b32_e32 v66, v243
	v_mov_b32_e32 v70, v246
	v_mov_b32_e32 v71, v247
	v_mov_b32_e32 v72, v248
	global_load_dword v114, v[244:245], off
	global_load_dword v115, v[244:245], off offset:128
	global_load_dword v116, v[244:245], off offset:256
	global_load_dword v117, v[244:245], off offset:384
	global_load_dword v118, v[244:245], off offset:512
	global_load_dword v119, v[244:245], off offset:640
	global_load_dword v120, v[244:245], off offset:768
	global_load_dword v121, v[244:245], off offset:896
	s_waitcnt vmcnt(40)
	v_cvt_pk_bf16_f32 v243, v74, v75
	s_nop 0
	v_lshlrev_b32_e32 v249, 16, v243
	v_and_b32_e32 v250, 0xffff0000, v243
	v_sub_f32_e32 v249, v74, v249
	v_sub_f32_e32 v250, v75, v250
	v_cvt_pk_bf16_f32 v246, v249, v250
	v_cvt_pk_bf16_f32 v75, v76, v77
	s_nop 0
	v_lshlrev_b32_e32 v249, 16, v75
	v_and_b32_e32 v250, 0xffff0000, v75
	v_sub_f32_e32 v249, v76, v249
	v_sub_f32_e32 v250, v77, v250
	v_cvt_pk_bf16_f32 v247, v249, v250
	v_cvt_pk_bf16_f32 v76, v78, v79
	s_nop 0
	v_lshlrev_b32_e32 v249, 16, v76
	v_and_b32_e32 v250, 0xffff0000, v76
	v_sub_f32_e32 v249, v78, v249
	v_sub_f32_e32 v250, v79, v250
	v_cvt_pk_bf16_f32 v248, v249, v250
	v_cvt_pk_bf16_f32 v77, v80, v81
	s_nop 0
	v_lshlrev_b32_e32 v249, 16, v77
	v_and_b32_e32 v250, 0xffff0000, v77
	v_sub_f32_e32 v249, v80, v249
	v_sub_f32_e32 v250, v81, v250
	v_cvt_pk_bf16_f32 v81, v249, v250
	v_mov_b32_e32 v74, v243
	v_mov_b32_e32 v78, v246
	v_mov_b32_e32 v79, v247
	v_mov_b32_e32 v80, v248
	global_load_dword v122, v[244:245], off offset:64
	global_load_dword v123, v[244:245], off offset:192
	global_load_dword v124, v[244:245], off offset:320
	global_load_dword v125, v[244:245], off offset:448
	global_load_dword v126, v[244:245], off offset:576
	global_load_dword v127, v[244:245], off offset:704
	global_load_dword v128, v[244:245], off offset:832
	global_load_dword v129, v[244:245], off offset:960
	s_waitcnt vmcnt(40)
	v_cvt_pk_bf16_f32 v243, v82, v83
	s_nop 0
	v_lshlrev_b32_e32 v249, 16, v243
	v_and_b32_e32 v250, 0xffff0000, v243
	v_sub_f32_e32 v249, v82, v249
	v_sub_f32_e32 v250, v83, v250
	v_cvt_pk_bf16_f32 v246, v249, v250
	v_cvt_pk_bf16_f32 v83, v84, v85
	s_nop 0
	v_lshlrev_b32_e32 v249, 16, v83
	v_and_b32_e32 v250, 0xffff0000, v83
	v_sub_f32_e32 v249, v84, v249
	v_sub_f32_e32 v250, v85, v250
	v_cvt_pk_bf16_f32 v247, v249, v250
	v_cvt_pk_bf16_f32 v84, v86, v87
	s_nop 0
	v_lshlrev_b32_e32 v249, 16, v84
	v_and_b32_e32 v250, 0xffff0000, v84
	v_sub_f32_e32 v249, v86, v249
	v_sub_f32_e32 v250, v87, v250
	v_cvt_pk_bf16_f32 v248, v249, v250
	v_cvt_pk_bf16_f32 v85, v88, v89
	s_nop 0
	v_lshlrev_b32_e32 v249, 16, v85
	v_and_b32_e32 v250, 0xffff0000, v85
	v_sub_f32_e32 v249, v88, v249
	v_sub_f32_e32 v250, v89, v250
	v_cvt_pk_bf16_f32 v89, v249, v250
	v_mov_b32_e32 v82, v243
	v_mov_b32_e32 v86, v246
	v_mov_b32_e32 v87, v247
	v_mov_b32_e32 v88, v248
	s_waitcnt vmcnt(32)
	v_cvt_pk_bf16_f32 v243, v90, v91
	s_nop 0
	v_lshlrev_b32_e32 v249, 16, v243
	v_and_b32_e32 v250, 0xffff0000, v243
	v_sub_f32_e32 v249, v90, v249
	v_sub_f32_e32 v250, v91, v250
	v_cvt_pk_bf16_f32 v246, v249, v250
	v_cvt_pk_bf16_f32 v91, v92, v93
	s_nop 0
	v_lshlrev_b32_e32 v249, 16, v91
	v_and_b32_e32 v250, 0xffff0000, v91
	v_sub_f32_e32 v249, v92, v249
	v_sub_f32_e32 v250, v93, v250
	v_cvt_pk_bf16_f32 v247, v249, v250
	v_cvt_pk_bf16_f32 v92, v94, v95
	s_nop 0
	v_lshlrev_b32_e32 v249, 16, v92
	v_and_b32_e32 v250, 0xffff0000, v92
	v_sub_f32_e32 v249, v94, v249
	v_sub_f32_e32 v250, v95, v250
	v_cvt_pk_bf16_f32 v248, v249, v250
	v_cvt_pk_bf16_f32 v93, v96, v97
	s_nop 0
	v_lshlrev_b32_e32 v249, 16, v93
	v_and_b32_e32 v250, 0xffff0000, v93
	v_sub_f32_e32 v249, v96, v249
	v_sub_f32_e32 v250, v97, v250
	v_cvt_pk_bf16_f32 v97, v249, v250
	v_mov_b32_e32 v90, v243
	v_mov_b32_e32 v94, v246
	v_mov_b32_e32 v95, v247
	v_mov_b32_e32 v96, v248
	s_waitcnt vmcnt(24)
	v_cvt_pk_bf16_f32 v243, v98, v99
	s_nop 0
	v_lshlrev_b32_e32 v249, 16, v243
	v_and_b32_e32 v250, 0xffff0000, v243
	v_sub_f32_e32 v249, v98, v249
	v_sub_f32_e32 v250, v99, v250
	v_cvt_pk_bf16_f32 v246, v249, v250
	v_cvt_pk_bf16_f32 v99, v100, v101
	s_nop 0
	v_lshlrev_b32_e32 v249, 16, v99
	v_and_b32_e32 v250, 0xffff0000, v99
	v_sub_f32_e32 v249, v100, v249
	v_sub_f32_e32 v250, v101, v250
	v_cvt_pk_bf16_f32 v247, v249, v250
	v_cvt_pk_bf16_f32 v100, v102, v103
	s_nop 0
	v_lshlrev_b32_e32 v249, 16, v100
	v_and_b32_e32 v250, 0xffff0000, v100
	v_sub_f32_e32 v249, v102, v249
	v_sub_f32_e32 v250, v103, v250
	v_cvt_pk_bf16_f32 v248, v249, v250
	v_cvt_pk_bf16_f32 v101, v104, v105
	s_nop 0
	v_lshlrev_b32_e32 v249, 16, v101
	v_and_b32_e32 v250, 0xffff0000, v101
	v_sub_f32_e32 v249, v104, v249
	v_sub_f32_e32 v250, v105, v250
	v_cvt_pk_bf16_f32 v105, v249, v250
	v_mov_b32_e32 v98, v243
	v_mov_b32_e32 v102, v246
	v_mov_b32_e32 v103, v247
	v_mov_b32_e32 v104, v248
	s_waitcnt vmcnt(16)
; __device__ __forceinline__ unsigned cvt_pk_bf16(float lo, float hi) { unsigned r; asm volatile("v_cvt_pk_bf16_f32 %0, %1, %2" : "=v"(r) : "v"(lo), "v"(hi)); return r; }
; #define P5_BAR() asm volatile("s_waitcnt lgkmcnt(0)\n\ts_barrier" ::: "memory")
; __device__ __forceinline__ void phase5(Frame& F, const Args& a) {
;     ...
; #pragma unroll
;         for (int sk = 0; sk < 8; ++sk)
; #pragma unroll
;             for (int nt = 0; nt < 2; ++nt) { float w8[8];
; #pragma unroll
;                 for (int t = 0; t < 8; ++t) w8[t] = wp[(size_t)(32 * sk + t) * NE + 16 * nt];
;                 pg8::u32x4 hv, lv;
; #pragma unroll
;                 for (int t2 = 0; t2 < 4; ++t2) { const unsigned h = pg8::cvt_pk_bf16(w8[2 * t2], w8[2 * t2 + 1]); hv[t2] = h; lv[t2] = pg8::cvt_pk_bf16(w8[2 * t2] - bflo(h), w8[2 * t2 + 1] - bfhi(h)); }
;                 wh[sk][nt] = __builtin_bit_cast(bf16x8_t, hv); wl[sk][nt] = __builtin_bit_cast(bf16x8_t, lv); } }
;     const float rbv = a.rb[lane & 31];
;     v2u ynx[8];
; #pragma unroll
;     for (int j = 0; j < 8; ++j) ynx[j] = *((const v2u*)(Y1 + (size_t)(row_base + wid) * D) + lane + 64 * j);
;     P5_BAR();
	v_cvt_pk_bf16_f32 v243, v106, v107
	s_nop 0
	v_lshlrev_b32_e32 v249, 16, v243
	v_and_b32_e32 v250, 0xffff0000, v243
	v_sub_f32_e32 v249, v106, v249
	v_sub_f32_e32 v250, v107, v250
	v_cvt_pk_bf16_f32 v246, v249, v250
	v_cvt_pk_bf16_f32 v107, v108, v109
	s_nop 0
	v_lshlrev_b32_e32 v249, 16, v107
	v_and_b32_e32 v250, 0xffff0000, v107
	v_sub_f32_e32 v249, v108, v249
	v_sub_f32_e32 v250, v109, v250
	v_cvt_pk_bf16_f32 v247, v249, v250
	v_cvt_pk_bf16_f32 v108, v110, v111
	s_nop 0
	v_lshlrev_b32_e32 v249, 16, v108
	v_and_b32_e32 v250, 0xffff0000, v108
	v_sub_f32_e32 v249, v110, v249
	v_sub_f32_e32 v250, v111, v250
	v_cvt_pk_bf16_f32 v248, v249, v250
	v_cvt_pk_bf16_f32 v109, v112, v113
	s_nop 0
	v_lshlrev_b32_e32 v249, 16, v109
	v_and_b32_e32 v250, 0xffff0000, v109
	v_sub_f32_e32 v249, v112, v249
	v_sub_f32_e32 v250, v113, v250
	v_cvt_pk_bf16_f32 v113, v249, v250
	v_mov_b32_e32 v106, v243
	v_mov_b32_e32 v110, v246
	v_mov_b32_e32 v111, v247
	v_mov_b32_e32 v112, v248
	s_waitcnt vmcnt(8)
	v_cvt_pk_bf16_f32 v243, v114, v115
	s_nop 0
	v_lshlrev_b32_e32 v249, 16, v243
	v_and_b32_e32 v250, 0xffff0000, v243
	v_sub_f32_e32 v249, v114, v249
	v_sub_f32_e32 v250, v115, v250
	v_cvt_pk_bf16_f32 v246, v249, v250
	v_cvt_pk_bf16_f32 v115, v116, v117
	s_nop 0
	v_lshlrev_b32_e32 v249, 16, v115
	v_and_b32_e32 v250, 0xffff0000, v115
	v_sub_f32_e32 v249, v116, v249
	v_sub_f32_e32 v250, v117, v250
	v_cvt_pk_bf16_f32 v247, v249, v250
	v_cvt_pk_bf16_f32 v116, v118, v119
	s_nop 0
	v_lshlrev_b32_e32 v249, 16, v116
	v_and_b32_e32 v250, 0xffff0000, v116
	v_sub_f32_e32 v249, v118, v249
	v_sub_f32_e32 v250, v119, v250
	v_cvt_pk_bf16_f32 v248, v249, v250
	v_cvt_pk_bf16_f32 v117, v120, v121
	s_nop 0
	v_lshlrev_b32_e32 v249, 16, v117
	v_and_b32_e32 v250, 0xffff0000, v117
	v_sub_f32_e32 v249, v120, v249
	v_sub_f32_e32 v250, v121, v250
	v_cvt_pk_bf16_f32 v121, v249, v250
	v_mov_b32_e32 v114, v243
	v_mov_b32_e32 v118, v246
	v_mov_b32_e32 v119, v247
	v_mov_b32_e32 v120, v248
	s_waitcnt vmcnt(0)
	v_cvt_pk_bf16_f32 v243, v122, v123
	s_nop 0
	v_lshlrev_b32_e32 v249, 16, v243
	v_and_b32_e32 v250, 0xffff0000, v243
	v_sub_f32_e32 v249, v122, v249
	v_sub_f32_e32 v250, v123, v250
	v_cvt_pk_bf16_f32 v246, v249, v250
	v_cvt_pk_bf16_f32 v123, v124, v125
	s_nop 0
	v_lshlrev_b32_e32 v249, 16, v123
	v_and_b32_e32 v250, 0xffff0000, v123
	v_sub_f32_e32 v249, v124, v249
	v_sub_f32_e32 v250, v125, v250
	v_cvt_pk_bf16_f32 v247, v249, v250
	v_cvt_pk_bf16_f32 v124, v126, v127
	s_nop 0
	v_lshlrev_b32_e32 v249, 16, v124
	v_and_b32_e32 v250, 0xffff0000, v124
	v_sub_f32_e32 v249, v126, v249
	v_sub_f32_e32 v250, v127, v250
	v_cvt_pk_bf16_f32 v248, v249, v250
	v_cvt_pk_bf16_f32 v125, v128, v129
	s_nop 0
	v_lshlrev_b32_e32 v249, 16, v125
	v_and_b32_e32 v250, 0xffff0000, v125
	v_sub_f32_e32 v249, v128, v249
	v_sub_f32_e32 v250, v129, v250
	v_cvt_pk_bf16_f32 v129, v249, v250
	v_mov_b32_e32 v122, v243
	v_mov_b32_e32 v126, v246
	v_mov_b32_e32 v127, v247
	v_mov_b32_e32 v128, v248
	s_waitcnt lgkmcnt(0)
	s_barrier
	s_cbranch_scc0 .LBB0_636
	s_add_u32 s20, s76, 0xa00000
	s_addc_u32 s21, s77, 0
	s_add_u32 s22, s76, 0xa40000
	s_addc_u32 s23, s77, 0
	v_lshlrev_b32_e32 v160, 4, v133
	s_add_i32 s4, 0, 0x19800
	v_add_u32_e32 v196, s4, v160
	s_add_i32 s4, 0, 0x1b800
	v_and_b32_e32 v136, 1, v138
	v_and_b32_e32 v134, 0x1f0, v130
	v_mov_b32_e32 v135, v141
	v_add_u32_e32 v197, s4, v160
	v_lshl_add_u64 v[134:135], s[76:77], 0, v[134:135]
	v_cmp_eq_u32_e64 s[4:5], 0, v136
	v_lshlrev_b32_e32 v136, 9, v136
	v_mov_b32_e32 v137, v141
	v_lshl_add_u64 v[134:135], v[134:135], 0, v[136:137]
	s_mov_b64 s[6:7], 0x24000000
	v_lshl_add_u64 v[158:159], v[134:135], 0, s[6:7]
	s_add_i32 s6, 0, 0x1d800
	v_add_u32_e32 v198, s6, v160
	s_add_i32 s6, 0, 0x1f800
	v_add_u32_e32 v199, s6, v160
	s_mul_i32 s6, s49, 0x1010
	v_lshlrev_b32_e32 v164, 2, v133
	s_add_i32 s6, s6, 0
	v_and_b32_e32 v136, 3, v138
	v_and_b32_e32 v134, 0xf0, v164
	v_mov_b32_e32 v135, v141
	s_add_i32 s19, 0, 0x10800
	v_add_u32_e32 v200, s6, v130
	v_lshl_add_u64 v[134:135], s[76:77], 0, v[134:135]
	v_cmp_gt_u32_e64 s[6:7], 2, v136
	v_lshlrev_b32_e32 v136, 8, v136
	s_lshl_b32 s26, s49, 10
	v_lshl_add_u64 v[134:135], v[134:135], 0, v[136:137]
	s_mov_b64 s[8:9], 0x5b000000
	s_lshl_b32 s24, s49, 7
	s_lshl_b32 s25, s49, 2
	s_add_i32 s26, s26, s19
	v_lshl_add_u64 v[160:161], v[134:135], 0, s[8:9]
	v_and_b32_e32 v134, 7, v138
	s_movk_i32 s10, 0x808
	s_add_u32 s35, s76, 0xe20000
	v_lshl_add_u32 v165, v1, 2, s19
	v_mad_u32_u24 v134, v134, s10, v140
	s_addc_u32 s36, s77, 0
	s_lshl_b32 s19, s49, 4
	v_lshl_add_u32 v201, v134, 1, 0
	v_lshlrev_b32_e32 v134, 9, v131
	v_mov_b32_e32 v131, v141
	s_add_i32 s19, s19, 0
	s_lshl_b32 s18, s18, 2
	v_lshl_add_u64 v[162:163], s[12:13], 0, v[130:131]
	v_lshl_add_u32 v130, v132, 2, s26
	v_add_u32_e32 v131, s19, v164
	s_add_i32 s18, s18, s25
	s_mov_b32 s34, 0
	v_cmp_eq_u32_e64 s[8:9], 0, v133
	v_cmp_gt_u32_e64 s[10:11], 32, v133
	v_cmp_gt_u32_e64 s[12:13], 4, v133
	v_cmp_eq_u32_e64 s[14:15], 1, v133
	v_cmp_eq_u32_e64 s[16:17], 2, v133
	v_add_u32_e32 v202, 0x18400, v131
	v_add_u32_e32 v164, s18, v133
	v_mov_b32_e32 v203, 0x3727c5ac
	s_mov_b32 s37, 0xf800000
	v_mov_b32_e32 v204, 0x260
	s_movk_i32 s38, 0x7fff
	s_mov_b32 s39, 0x1e3ce508
	s_mov_b32 s40, 0x42fe0000
	s_mov_b32 s41, 0x4b3fff81
	s_mov_b32 s42, 0xc0c0400
	s_mov_b32 s43, 0x4000c0c
	v_add_u32_e32 v205, v130, v134
	v_add_u32_e32 v206, s24, v165
	v_mov_b32_e32 v207, 1
	v_mov_b32_e32 v208, 0x4b40007f
	v_mov_b32_e32 v209, 0xff61b1e6
	s_branch .LBB0_627
